# GLA-B: second half's tile loads issued before the first half's store loop (into registers unused in this phase) and collected with vmcnt(32) instead of being issued after it
# baseline (speedup 1.0000x reference)
.LBB0_1053:
	s_nop 0
	s_nop 0
	s_nop 0
	s_nop 0
	s_nop 0
	s_nop 0
	v_and_b32_e32 v3, 64, v68
	v_xor_b32_e32 v2, 32, v68
	v_add_u32_e32 v3, 64, v3
	v_cmp_lt_i32_e32 vcc, v2, v3
	s_mov_b64 s[20:21], -1
	s_mov_b64 s[22:23], -1
	v_cndmask_b32_e32 v2, v68, v2, vcc
	v_lshlrev_b32_e32 v2, 2, v2
	ds_bpermute_b32 v6, v2, v71
	ds_bpermute_b32 v5, v2, v50
	ds_bpermute_b32 v3, v2, v57
	ds_bpermute_b32 v7, v2, v69
	ds_bpermute_b32 v4, v2, v59
	ds_bpermute_b32 v2, v2, v70
	s_waitcnt lgkmcnt(5)
	v_cmp_nlt_f32_e32 vcc, v71, v6
	s_and_saveexec_b64 s[18:19], vcc
	s_cbranch_execz .LBB0_1057
	v_cmp_eq_f32_e32 vcc, v71, v6
	s_mov_b64 s[22:23], 0
	s_and_saveexec_b64 s[24:25], vcc
	s_cbranch_execz .LBB0_1056
	s_waitcnt lgkmcnt(2)
	v_cmp_lt_i32_e32 vcc, v7, v69
	s_and_b64 s[22:23], vcc, exec

.LBB0_1176:
	s_or_b64 exec, exec, s[20:21]
	v_add_u32_e32 v34, s33, v87
	v_add_u32_e32 v36, s33, v88
	v_add_u32_e32 v38, s33, v89
	v_add_u32_e32 v40, s33, v90
	v_add_u32_e32 v42, s33, v91
	v_add_u32_e32 v44, s33, v92
	v_add_u32_e32 v46, s33, v93
	v_add_u32_e32 v48, s33, v86
	s_lshl_b32 s0, s28, 1
	v_ashrrev_i32_e32 v35, 31, v34
	v_ashrrev_i32_e32 v37, 31, v36
	v_ashrrev_i32_e32 v39, 31, v38
	v_ashrrev_i32_e32 v41, 31, v40
	v_ashrrev_i32_e32 v43, 31, v42
	v_ashrrev_i32_e32 v45, 31, v44
	v_ashrrev_i32_e32 v47, 31, v46
	v_ashrrev_i32_e32 v49, 31, v48
	s_and_b32 s0, s0, 0x3f00
	v_lshlrev_b64 v[34:35], 14, v[34:35]
	v_lshlrev_b64 v[36:37], 14, v[36:37]
	v_lshlrev_b64 v[38:39], 14, v[38:39]
	v_lshlrev_b64 v[40:41], 14, v[40:41]
	v_lshlrev_b64 v[42:43], 14, v[42:43]
	v_lshlrev_b64 v[44:45], 14, v[44:45]
	v_lshlrev_b64 v[46:47], 14, v[46:47]
	v_lshlrev_b64 v[48:49], 14, v[48:49]
	v_or_b32_e32 v34, s0, v34
	v_or_b32_e32 v36, s0, v36
	v_or_b32_e32 v38, s0, v38
	v_or_b32_e32 v40, s0, v40
	v_or_b32_e32 v42, s0, v42
	v_or_b32_e32 v44, s0, v44
	v_or_b32_e32 v46, s0, v46
	v_or_b32_e32 v48, s0, v48
	v_lshl_add_u64 v[50:51], s[14:15], 0, v[34:35]
	v_lshl_add_u64 v[52:53], s[14:15], 0, v[36:37]
	v_lshl_add_u64 v[54:55], s[14:15], 0, v[38:39]
	v_lshl_add_u64 v[56:57], s[14:15], 0, v[40:41]
	v_lshl_add_u64 v[58:59], s[14:15], 0, v[42:43]
	v_lshl_add_u64 v[60:61], s[14:15], 0, v[44:45]
	v_lshl_add_u64 v[62:63], s[14:15], 0, v[46:47]
	v_lshl_add_u64 v[64:65], s[14:15], 0, v[48:49]
	v_mov_b32_e32 v94, 1.0
	s_movk_i32 s0, 0xe000
	s_or_b32 s98, s10, 0x80
	s_mov_b32 s99, s11
	v_lshl_add_u64 v[216:217], v[20:21], 0, v[26:27]
	v_lshl_add_u64 v[216:217], v[216:217], 0, s[98:99]
	global_load_dwordx4 v[200:203], v[216:217], off
	v_lshl_add_u64 v[216:217], v[20:21], 0, v[30:31]
	v_lshl_add_u64 v[216:217], v[216:217], 0, s[98:99]
	global_load_dwordx4 v[204:207], v[216:217], off
	v_lshl_add_u64 v[216:217], v[20:21], 0, v[28:29]
	v_lshl_add_u64 v[216:217], v[216:217], 0, s[98:99]
	global_load_dwordx4 v[208:211], v[216:217], off
	v_lshl_add_u64 v[216:217], v[20:21], 0, v[32:33]
	v_lshl_add_u64 v[216:217], v[216:217], 0, s[98:99]
	global_load_dwordx4 v[212:215], v[216:217], off
.LBB0_1177:
	v_add_u32_e32 v95, s0, v84
	ds_read2st64_b32 v[112:113], v95 offset0:32 offset1:33
	ds_read2st64_b32 v[114:115], v95 offset0:34 offset1:35
	ds_read2st64_b32 v[116:117], v95 offset0:36 offset1:37
	ds_read2st64_b32 v[118:119], v95 offset0:38 offset1:39
	v_add_u32_e32 v120, 0x12000, v95
	v_add_u32_e32 v121, 0x12100, v95
	v_add_u32_e32 v122, 0x12200, v95
	v_add_u32_e32 v123, 0x12300, v95
	v_add_u32_e32 v124, 0x12400, v95
	v_add_u32_e32 v125, 0x12500, v95
	v_add_u32_e32 v126, 0x12600, v95
	v_add_u32_e32 v95, 0x12700, v95
	ds_read_b32 v120, v120
	ds_read_b32 v121, v121
	ds_read_b32 v122, v122
	ds_read_b32 v123, v123
	ds_read_b32 v124, v124
	ds_read_b32 v125, v125
	ds_read_b32 v126, v126
	ds_read_b32 v95, v95
	s_waitcnt lgkmcnt(11)
	v_fma_f32 v112, v25, v94, v112
	s_waitcnt lgkmcnt(7)
	v_mul_f32_e32 v94, v94, v120
	v_bfe_u32 v120, v112, 16, 1
	v_lshl_add_u64 v[96:97], v[64:65], 0, v[22:23]
	v_add3_u32 v112, v112, v120, s30
	v_fmac_f32_e32 v113, v25, v94
	s_waitcnt lgkmcnt(6)
	v_mul_f32_e32 v94, v94, v121
	global_store_short_d16_hi v[96:97], v112, off
	v_bfe_u32 v96, v113, 16, 1
	v_fma_f32 v97, v25, v94, v114
	s_waitcnt lgkmcnt(5)
	v_mul_f32_e32 v94, v94, v122
	v_lshl_add_u64 v[98:99], v[62:63], 0, v[22:23]
	v_add3_u32 v96, v113, v96, s30
	v_bfe_u32 v112, v97, 16, 1
	v_fmac_f32_e32 v115, v25, v94
	s_waitcnt lgkmcnt(4)
	v_mul_f32_e32 v94, v94, v123
	v_lshl_add_u64 v[100:101], v[60:61], 0, v[22:23]
	global_store_short_d16_hi v[98:99], v96, off
	v_add3_u32 v96, v97, v112, s30
	v_bfe_u32 v97, v115, 16, 1
	v_fma_f32 v98, v25, v94, v116
	s_waitcnt lgkmcnt(3)
	v_mul_f32_e32 v94, v94, v124
	v_lshl_add_u64 v[102:103], v[58:59], 0, v[22:23]
	global_store_short_d16_hi v[100:101], v96, off
	v_add3_u32 v96, v115, v97, s30
	v_bfe_u32 v97, v98, 16, 1
	v_fmac_f32_e32 v117, v25, v94
	s_waitcnt lgkmcnt(2)
	v_mul_f32_e32 v94, v94, v125
	v_lshl_add_u64 v[104:105], v[56:57], 0, v[22:23]
	global_store_short_d16_hi v[102:103], v96, off
	v_add3_u32 v96, v98, v97, s30
	v_bfe_u32 v97, v117, 16, 1
	v_fma_f32 v98, v25, v94, v118
	s_waitcnt lgkmcnt(1)
	v_mul_f32_e32 v94, v94, v126
	v_lshl_add_u64 v[106:107], v[54:55], 0, v[22:23]
	global_store_short_d16_hi v[104:105], v96, off
	v_add3_u32 v96, v117, v97, s30
	v_bfe_u32 v97, v98, 16, 1
	v_fmac_f32_e32 v119, v25, v94
	v_lshl_add_u64 v[108:109], v[52:53], 0, v[22:23]
	s_addk_i32 s0, 0x800
	s_waitcnt lgkmcnt(0)
	v_mul_f32_e32 v94, v94, v95
	global_store_short_d16_hi v[106:107], v96, off
	v_add3_u32 v95, v98, v97, s30
	v_bfe_u32 v96, v119, 16, 1
	v_lshl_add_u64 v[110:111], v[50:51], 0, v[22:23]
	v_lshl_add_u64 v[50:51], v[50:51], 0, s[18:19]
	v_lshl_add_u64 v[52:53], v[52:53], 0, s[18:19]
	v_lshl_add_u64 v[54:55], v[54:55], 0, s[18:19]
	v_lshl_add_u64 v[56:57], v[56:57], 0, s[18:19]
	v_lshl_add_u64 v[58:59], v[58:59], 0, s[18:19]
	v_lshl_add_u64 v[60:61], v[60:61], 0, s[18:19]
	v_lshl_add_u64 v[62:63], v[62:63], 0, s[18:19]
	v_lshl_add_u64 v[64:65], v[64:65], 0, s[18:19]
	s_cmp_eq_u32 s0, 0
	global_store_short_d16_hi v[108:109], v95, off
	v_add3_u32 v95, v119, v96, s30
	global_store_short_d16_hi v[110:111], v95, off
	s_cbranch_scc0 .LBB0_1177
	s_bitset1_b32 s10, 7
	s_waitcnt lgkmcnt(0)
	s_barrier
	v_mov_b32_e32 v25, 1.0
	s_mov_b32 s0, 0
	s_waitcnt vmcnt(32)
	v_mov_b32_e32 v50, v200
	v_mov_b32_e32 v51, v201
	v_mov_b32_e32 v52, v202
	v_mov_b32_e32 v53, v203
	v_mov_b32_e32 v54, v204
	v_mov_b32_e32 v55, v205
	v_mov_b32_e32 v56, v206
	v_mov_b32_e32 v57, v207
	v_mov_b32_e32 v26, v208
	v_mov_b32_e32 v27, v209
	v_mov_b32_e32 v28, v210
	v_mov_b32_e32 v29, v211
	v_mov_b32_e32 v30, v212
	v_mov_b32_e32 v31, v213
	v_mov_b32_e32 v32, v214
	v_mov_b32_e32 v33, v215
	v_lshlrev_b32_e32 v58, 16, v50
	v_and_b32_e32 v59, 0xffff0000, v50
	v_lshlrev_b32_e32 v60, 16, v51
	v_and_b32_e32 v61, 0xffff0000, v51
	v_lshlrev_b32_e32 v50, 16, v52
	v_and_b32_e32 v51, 0xffff0000, v52
	v_lshlrev_b32_e32 v52, 16, v53
	v_and_b32_e32 v53, 0xffff0000, v53
	v_lshlrev_b32_e32 v62, 16, v26
	v_and_b32_e32 v63, 0xffff0000, v26
	v_lshlrev_b32_e32 v64, 16, v27
	v_and_b32_e32 v65, 0xffff0000, v27
	v_lshlrev_b32_e32 v26, 16, v28
	v_and_b32_e32 v27, 0xffff0000, v28
	v_lshlrev_b32_e32 v28, 16, v29
	v_and_b32_e32 v29, 0xffff0000, v29
	v_lshlrev_b32_e32 v94, 16, v54
	v_and_b32_e32 v95, 0xffff0000, v54
	v_lshlrev_b32_e32 v96, 16, v55
	v_and_b32_e32 v97, 0xffff0000, v55
	v_lshlrev_b32_e32 v54, 16, v56
	v_and_b32_e32 v55, 0xffff0000, v56
	v_lshlrev_b32_e32 v56, 16, v57
	v_and_b32_e32 v57, 0xffff0000, v57
	v_lshlrev_b32_e32 v98, 16, v30
	v_and_b32_e32 v99, 0xffff0000, v30
	v_lshlrev_b32_e32 v100, 16, v31
	v_and_b32_e32 v101, 0xffff0000, v31
	v_lshlrev_b32_e32 v30, 16, v32
	v_and_b32_e32 v31, 0xffff0000, v32
	v_lshlrev_b32_e32 v32, 16, v33
	v_and_b32_e32 v33, 0xffff0000, v33
	ds_write_b128 v77, v[58:61]
	ds_write_b128 v77, v[50:53] offset:16
	ds_write_b128 v79, v[62:65]
	ds_write_b128 v79, v[26:29] offset:16
	ds_write_b128 v81, v[94:97]
	ds_write_b128 v81, v[54:57] offset:16
	ds_write_b128 v83, v[98:101]
	ds_write_b128 v83, v[30:33] offset:16
	s_waitcnt lgkmcnt(0)
	s_barrier
	v_mov_b32_e32 v27, 0
